# baseline (speedup 1.0000x reference)
.LBB2_24:
	s_or_b64 exec, exec, s[6:7]
	s_and_saveexec_b64 s[4:5], s[0:1]
	v_sub_u32_e32 v8, v10, v12
	v_add_u32_e32 v8, v11, v8
	v_add_u32_e32 v9, v8, v9
	ds_write_b64 v7, v[8:9] offset:3328
	ds_write_b64 v7, v[8:9] offset:2560
	s_or_b64 exec, exec, s[4:5]
	v_lshrrev_b32_e32 v25, 3, v0
	v_lshlrev_b32_e32 v10, 2, v25
	v_add_u32_e32 v7, v3, v2
	s_waitcnt lgkmcnt(0)
	s_barrier
	ds_read2_b32 v[8:9], v10 offset1:32
	ds_read2_b32 v[2:3], v10 offset0:64 offset1:96
	v_add_u32_e32 v4, v7, v4
	v_add_u32_e32 v12, v4, v5
	ds_read2_b32 v[4:5], v10 offset0:128 offset1:160
	ds_read2_b32 v[10:11], v10 offset0:192 offset1:224
	s_waitcnt lgkmcnt(3)
	v_max_u32_sdwa v14, v9, v8 dst_sel:DWORD dst_unused:UNUSED_PAD src0_sel:WORD_1 src1_sel:WORD_1
	s_waitcnt lgkmcnt(2)
	v_lshrrev_b32_e32 v7, 16, v2
	v_lshrrev_b32_e32 v13, 16, v3
	v_max3_u32 v16, v13, v7, v14
	s_waitcnt lgkmcnt(1)
	v_lshrrev_b32_e32 v14, 16, v4
	v_lshrrev_b32_e32 v15, 16, v5
	v_max3_u32 v18, v15, v14, v16
	s_waitcnt lgkmcnt(0)
	v_lshrrev_b32_e32 v16, 16, v10
	v_lshrrev_b32_e32 v17, 16, v11
	v_max3_u32 v18, v17, v16, v18
	v_and_b32_e32 v19, 7, v0
	v_cmp_lt_u32_e64 s[0:1], v19, v18
	s_and_saveexec_b64 s[62:63], s[0:1]
	s_cbranch_execz .LBB2_77
	v_mul_u32_u24_e32 v21, 0xc35, v25
	v_and_b32_e32 v22, 0xffff, v9
	s_mov_b32 s1, 0x186a0
	s_movk_i32 s0, 0xc35
	v_add3_u32 v21, v21, v22, s1
	v_mov_b32_e32 v22, 0x30d40
	v_mad_u32_u24 v23, v25, s0, v22
	v_add_u32_sdwa v22, v2, v23 dst_sel:DWORD dst_unused:UNUSED_PAD src0_sel:WORD_0 src1_sel:DWORD
	v_and_b32_e32 v2, 0xffff, v3
	v_add3_u32 v23, v23, v2, s1
	v_mov_b32_e32 v2, 0x61a80
	v_mad_u32_u24 v2, v25, s0, v2
	v_and_b32_e32 v3, 0xffff, v5
	v_add_u32_sdwa v4, v4, v2 dst_sel:DWORD dst_unused:UNUSED_PAD src0_sel:WORD_0 src1_sel:DWORD
	v_add3_u32 v5, v2, v3, s1
	v_mov_b32_e32 v2, 0x927c0
	v_and_b32_e32 v20, 0xffff, v8
	v_mad_u32_u24 v2, v25, s0, v2
	v_and_b32_e32 v3, 0xffff, v11
	v_mad_u32_u24 v20, v25, s0, v20
	v_add_u32_sdwa v10, v10, v2 dst_sel:DWORD dst_unused:UNUSED_PAD src0_sel:WORD_0 src1_sel:DWORD
	v_add3_u32 v11, v2, v3, s1
	v_or_b32_e32 v24, 0x80, v24
	s_mov_b64 s[64:65], 0
	v_mov_b32_e32 v3, 0
	v_mov_b32_e32 v25, 1
	s_branch .LBB2_29

.LBB2_29:
	v_cmp_lt_u32_sdwa s[0:1], v19, v8 src0_sel:DWORD src1_sel:WORD_1
	v_add_u32_e32 v42, 8, v19
	v_cmp_lt_u32_sdwa s[30:31], v42, v8 src0_sel:DWORD src1_sel:WORD_1
	v_cndmask_b32_e64 v2, 0, v19, s[0:1]
	v_add_u32_e32 v2, v2, v20
	v_lshl_add_u64 v[26:27], v[2:3], 2, s[60:61]
	v_cndmask_b32_e64 v2, 0, v42, s[30:31]
	v_add_u32_e32 v43, 16, v19
	v_add_u32_e32 v2, v2, v20
	v_cmp_lt_u32_sdwa s[4:5], v43, v8 src0_sel:DWORD src1_sel:WORD_1
	v_lshl_add_u64 v[28:29], v[2:3], 2, s[60:61]
	v_cmp_lt_u32_sdwa s[6:7], v19, v9 src0_sel:DWORD src1_sel:WORD_1
	v_cndmask_b32_e64 v2, 0, v43, s[4:5]
	v_add_u32_e32 v2, v2, v20
	v_lshl_add_u64 v[30:31], v[2:3], 2, s[60:61]
	v_cndmask_b32_e64 v2, 0, v19, s[6:7]
	v_add_u32_e32 v2, v2, v21
	v_cmp_lt_u32_sdwa s[8:9], v42, v9 src0_sel:DWORD src1_sel:WORD_1
	v_lshl_add_u64 v[32:33], v[2:3], 2, s[60:61]
	v_cmp_lt_u32_sdwa s[10:11], v43, v9 src0_sel:DWORD src1_sel:WORD_1
	v_cndmask_b32_e64 v2, 0, v42, s[8:9]
	v_add_u32_e32 v2, v2, v21
	v_lshl_add_u64 v[34:35], v[2:3], 2, s[60:61]
	v_cndmask_b32_e64 v2, 0, v43, s[10:11]
	v_add_u32_e32 v2, v2, v21
	v_cmp_lt_u32_e64 s[12:13], v19, v7
	v_lshl_add_u64 v[36:37], v[2:3], 2, s[60:61]
	v_cmp_lt_u32_e64 s[14:15], v42, v7
	v_cndmask_b32_e64 v2, 0, v19, s[12:13]
	v_add_u32_e32 v2, v2, v22
	v_lshl_add_u64 v[38:39], v[2:3], 2, s[60:61]
	v_cndmask_b32_e64 v2, 0, v42, s[14:15]
	v_add_u32_e32 v2, v2, v22
	v_cmp_lt_u32_e64 s[16:17], v43, v7
	v_lshl_add_u64 v[40:41], v[2:3], 2, s[60:61]
	v_cmp_lt_u32_e64 s[18:19], v19, v13
	v_cndmask_b32_e64 v2, 0, v43, s[16:17]
	v_add_u32_e32 v2, v2, v22
	global_load_dword v44, v[26:27], off
	global_load_dword v45, v[28:29], off
	global_load_dword v46, v[30:31], off
	global_load_dword v47, v[32:33], off
	s_waitcnt lgkmcnt(5)
	global_load_dword v49, v[34:35], off
	s_waitcnt lgkmcnt(4)
	global_load_dword v50, v[36:37], off
	global_load_dword v51, v[38:39], off
	global_load_dword v52, v[40:41], off
	v_lshl_add_u64 v[26:27], v[2:3], 2, s[60:61]
	v_cndmask_b32_e64 v2, 0, v19, s[18:19]
	v_add_u32_e32 v2, v2, v23
	v_cmp_lt_u32_e64 s[20:21], v42, v13
	v_lshl_add_u64 v[28:29], v[2:3], 2, s[60:61]
	v_cmp_lt_u32_e64 s[22:23], v43, v13
	v_cndmask_b32_e64 v2, 0, v42, s[20:21]
	v_add_u32_e32 v2, v2, v23
	v_lshl_add_u64 v[30:31], v[2:3], 2, s[60:61]
	v_cndmask_b32_e64 v2, 0, v43, s[22:23]
	v_add_u32_e32 v2, v2, v23
	v_cmp_lt_u32_e64 s[24:25], v19, v14
	v_lshl_add_u64 v[32:33], v[2:3], 2, s[60:61]
	v_cmp_lt_u32_e64 s[26:27], v42, v14
	v_cndmask_b32_e64 v2, 0, v19, s[24:25]
	v_add_u32_e32 v2, v2, v4
	v_lshl_add_u64 v[34:35], v[2:3], 2, s[60:61]
	v_cndmask_b32_e64 v2, 0, v42, s[26:27]
	v_add_u32_e32 v2, v2, v4
	v_cmp_lt_u32_e64 s[28:29], v43, v14
	v_lshl_add_u64 v[36:37], v[2:3], 2, s[60:61]
	v_cmp_lt_u32_e64 s[34:35], v19, v15
	v_cndmask_b32_e64 v2, 0, v43, s[28:29]
	v_add_u32_e32 v2, v2, v4
	v_lshl_add_u64 v[38:39], v[2:3], 2, s[60:61]
	v_cndmask_b32_e64 v2, 0, v19, s[34:35]
	v_add_u32_e32 v2, v2, v5
	v_cmp_lt_u32_e64 s[36:37], v42, v15
	v_lshl_add_u64 v[40:41], v[2:3], 2, s[60:61]
	v_cmp_lt_u32_e64 s[38:39], v43, v15
	v_cndmask_b32_e64 v2, 0, v42, s[36:37]
	v_add_u32_e32 v2, v2, v5
	s_waitcnt lgkmcnt(1)
	global_load_dword v53, v[26:27], off
	global_load_dword v54, v[28:29], off
	s_waitcnt lgkmcnt(0)
	global_load_dword v55, v[30:31], off
	global_load_dword v56, v[32:33], off
	global_load_dword v57, v[34:35], off
	global_load_dword v58, v[36:37], off
	global_load_dword v59, v[38:39], off
	global_load_dword v60, v[40:41], off
	v_lshl_add_u64 v[26:27], v[2:3], 2, s[60:61]
	v_cndmask_b32_e64 v2, 0, v43, s[38:39]
	v_add_u32_e32 v2, v2, v5
	v_cmp_lt_u32_e64 s[40:41], v19, v16
	v_lshl_add_u64 v[28:29], v[2:3], 2, s[60:61]
	v_cmp_lt_u32_e64 s[42:43], v42, v16
	v_cndmask_b32_e64 v2, 0, v19, s[40:41]
	v_add_u32_e32 v2, v2, v10
	v_lshl_add_u64 v[30:31], v[2:3], 2, s[60:61]
	v_cndmask_b32_e64 v2, 0, v42, s[42:43]
	v_add_u32_e32 v2, v2, v10
	v_cmp_lt_u32_e64 s[44:45], v43, v16
	v_lshl_add_u64 v[32:33], v[2:3], 2, s[60:61]
	v_cmp_lt_u32_e64 s[46:47], v19, v17
	v_cndmask_b32_e64 v2, 0, v43, s[44:45]
	v_add_u32_e32 v2, v2, v10
	v_lshl_add_u64 v[34:35], v[2:3], 2, s[60:61]
	v_cndmask_b32_e64 v2, 0, v19, s[46:47]
	v_add_u32_e32 v2, v2, v11
	v_cmp_lt_u32_e64 s[48:49], v42, v17
	v_lshl_add_u64 v[36:37], v[2:3], 2, s[60:61]
	v_cmp_lt_u32_e64 s[50:51], v43, v17
	v_cndmask_b32_e64 v2, 0, v42, s[48:49]
	v_add_u32_e32 v2, v2, v11
	v_lshl_add_u64 v[38:39], v[2:3], 2, s[60:61]
	v_cndmask_b32_e64 v2, 0, v43, s[50:51]
	v_add_u32_e32 v2, v2, v11
	v_lshl_add_u64 v[40:41], v[2:3], 2, s[60:61]
	global_load_dword v2, v[26:27], off
	s_nop 0
	global_load_dword v26, v[28:29], off
	global_load_dword v42, v[30:31], off
	s_nop 0
	global_load_dword v33, v[32:33], off
	s_nop 0
	global_load_dword v61, v[34:35], off
	global_load_dword v62, v[36:37], off
	global_load_dword v63, v[38:39], off
	global_load_dword v64, v[40:41], off
	s_waitcnt vmcnt(23)
	v_cndmask_b32_e64 v48, -1, v44, s[0:1]
	s_waitcnt vmcnt(22)
	v_cndmask_b32_e64 v40, -1, v45, s[30:31]
	s_waitcnt vmcnt(21)
	v_cndmask_b32_e64 v32, -1, v46, s[4:5]
	s_waitcnt vmcnt(20)
	v_cndmask_b32_e64 v47, -1, v47, s[6:7]
	s_waitcnt vmcnt(19)
	v_cndmask_b32_e64 v39, -1, v49, s[8:9]
	s_waitcnt vmcnt(18)
	v_cndmask_b32_e64 v31, -1, v50, s[10:11]
	v_and_b32_e32 v50, 0xffff, v47
	s_waitcnt vmcnt(17)
	v_cndmask_b32_e64 v46, -1, v51, s[12:13]
	s_waitcnt vmcnt(16)
	v_cndmask_b32_e64 v38, -1, v52, s[14:15]
	v_cmp_eq_u32_e64 s[0:1], -1, v46
	v_cmp_eq_u32_e64 s[12:13], -1, v40
	v_cmp_eq_u32_e64 s[14:15], -1, v39
	v_and_b32_e32 v49, 0xffff, v48
	v_bfe_u32 v70, v48, 16, 7
	s_waitcnt vmcnt(15)
	v_cndmask_b32_e64 v30, -1, v53, s[16:17]
	s_waitcnt vmcnt(14)
	v_cndmask_b32_e64 v45, -1, v54, s[18:19]
	v_cmp_eq_u32_e64 s[18:19], -1, v47
	s_waitcnt vmcnt(12)
	v_cndmask_b32_e64 v29, -1, v56, s[22:23]
	s_waitcnt vmcnt(11)
	v_cndmask_b32_e64 v44, -1, v57, s[24:25]
	v_cndmask_b32_e64 v50, v50, 0, s[18:19]
	v_lshlrev_b32_e32 v52, 3, v50
	v_and_b32_e32 v50, 0xffff, v46
	v_cndmask_b32_e64 v50, v50, 0, s[0:1]
	v_lshlrev_b32_e32 v54, 3, v50
	v_and_b32_e32 v50, 0xffff, v45
	v_cmp_eq_u32_e64 s[4:5], -1, v44
	s_waitcnt vmcnt(8)
	v_cndmask_b32_e64 v43, -1, v60, s[34:35]
	v_cndmask_b32_e64 v36, -1, v58, s[26:27]
	v_cmp_eq_u32_e64 s[6:7], -1, v43
	v_cndmask_b32_e64 v37, -1, v55, s[20:21]
	v_cmp_eq_u32_e64 s[20:21], -1, v48
	v_cndmask_b32_e64 v28, -1, v59, s[28:29]
	v_cmp_eq_u32_e64 s[16:17], -1, v38
	v_cndmask_b32_e64 v49, v49, 0, s[20:21]
	v_and_b32_e32 v55, 0xffff, v36
	v_cmp_eq_u32_e64 s[34:35], -1, v30
	v_lshlrev_b32_e32 v49, 3, v49
	v_and_b32_e32 v65, 0xffff, v29
	v_cmp_eq_u32_e64 s[30:31], -1, v29
	v_cmp_eq_u32_e64 s[28:29], -1, v28
	v_cndmask_b32_e64 v70, v70, v24, s[20:21]
	v_cndmask_b32_e64 v65, v65, 0, s[30:31]
	v_lshlrev_b32_e32 v81, 3, v65
	s_waitcnt vmcnt(7)
	v_cndmask_b32_e64 v35, -1, v2, s[36:37]
	s_waitcnt vmcnt(6)
	v_cndmask_b32_e64 v27, -1, v26, s[38:39]
	s_waitcnt vmcnt(5)
	v_cndmask_b32_e64 v42, -1, v42, s[40:41]
	v_cmp_eq_u32_e64 s[8:9], -1, v42
	s_waitcnt vmcnt(4)
	v_cndmask_b32_e64 v34, -1, v33, s[42:43]
	s_waitcnt vmcnt(2)
	v_cndmask_b32_e64 v41, -1, v62, s[46:47]
	v_cmp_eq_u32_e64 s[10:11], -1, v41
	s_waitcnt vmcnt(0)
	v_cndmask_b32_e64 v2, -1, v64, s[50:51]
	v_cmp_eq_u32_e64 s[50:51], -1, v45
	v_cndmask_b32_e64 v33, -1, v63, s[48:49]
	v_cmp_eq_u32_e64 s[46:47], -1, v36
	v_cndmask_b32_e64 v50, v50, 0, s[50:51]
	v_lshlrev_b32_e32 v56, 3, v50
	v_and_b32_e32 v50, 0xffff, v44
	v_cndmask_b32_e64 v50, v50, 0, s[4:5]
	v_lshlrev_b32_e32 v58, 3, v50
	v_and_b32_e32 v50, 0xffff, v43
	v_cndmask_b32_e64 v50, v50, 0, s[6:7]
	v_lshlrev_b32_e32 v60, 3, v50
	v_and_b32_e32 v50, 0xffff, v42
	v_cndmask_b32_e64 v50, v50, 0, s[8:9]
	v_lshlrev_b32_e32 v62, 3, v50
	v_and_b32_e32 v50, 0xffff, v41
	v_cndmask_b32_e64 v50, v50, 0, s[10:11]
	v_lshlrev_b32_e32 v64, 3, v50
	v_and_b32_e32 v50, 0xffff, v40
	v_cndmask_b32_e64 v50, v50, 0, s[12:13]
	v_lshlrev_b32_e32 v66, 3, v50
	v_and_b32_e32 v50, 0xffff, v39
	v_cndmask_b32_e64 v50, v50, 0, s[14:15]
	v_lshlrev_b32_e32 v68, 3, v50
	v_and_b32_e32 v50, 0xffff, v38
	v_and_b32_e32 v59, 0xffff, v33
	v_cmp_eq_u32_e64 s[40:41], -1, v33
	v_and_b32_e32 v63, 0xffff, v30
	v_cndmask_b32_e64 v53, v50, 0, s[16:17]
	v_cndmask_b32_e64 v55, v55, 0, s[46:47]
	v_cndmask_b32_e64 v59, v59, 0, s[40:41]
	v_cndmask_b32_e64 v63, v63, 0, s[34:35]
	global_load_dwordx2 v[50:51], v49, s[58:59]
	v_cmp_eq_u32_e64 s[48:49], -1, v37
	v_lshlrev_b32_e32 v74, 3, v55
	global_load_dwordx2 v[54:55], v54, s[58:59]
	v_lshlrev_b32_e32 v77, 3, v59
	global_load_dwordx2 v[58:59], v58, s[58:59]
	v_lshlrev_b32_e32 v80, 3, v63
	global_load_dwordx2 v[62:63], v62, s[58:59]
	v_lshlrev_b32_e32 v49, 3, v53
	v_and_b32_e32 v53, 0xffff, v37
	v_cndmask_b32_e64 v53, v53, 0, s[48:49]
	v_lshlrev_b32_e32 v72, 3, v53
	global_load_dwordx2 v[52:53], v52, s[58:59]
	v_cndmask_b32_e64 v26, -1, v61, s[44:45]
	v_and_b32_e32 v57, 0xffff, v35
	v_cmp_eq_u32_e64 s[44:45], -1, v35
	v_cmp_eq_u32_e64 s[42:43], -1, v34
	v_and_b32_e32 v61, 0xffff, v32
	v_cndmask_b32_e64 v57, v57, 0, s[44:45]
	v_lshlrev_b32_e32 v75, 3, v57
	v_and_b32_e32 v57, 0xffff, v34
	v_cndmask_b32_e64 v57, v57, 0, s[42:43]
	v_lshlrev_b32_e32 v76, 3, v57
	global_load_dwordx2 v[56:57], v56, s[58:59]
	v_cmp_eq_u32_e64 s[38:39], -1, v32
	v_cmp_eq_u32_e64 s[36:37], -1, v31
	v_and_b32_e32 v65, 0xffff, v28
	v_cndmask_b32_e64 v61, v61, 0, s[38:39]
	v_lshlrev_b32_e32 v78, 3, v61
	v_and_b32_e32 v61, 0xffff, v31
	v_cndmask_b32_e64 v61, v61, 0, s[36:37]
	v_lshlrev_b32_e32 v79, 3, v61
	global_load_dwordx2 v[60:61], v60, s[58:59]
	v_cndmask_b32_e64 v65, v65, 0, s[28:29]
	v_lshlrev_b32_e32 v82, 3, v65
	global_load_dwordx2 v[64:65], v64, s[58:59]
	v_and_b32_e32 v67, 0xffff, v27
	v_cmp_eq_u32_e64 s[26:27], -1, v27
	v_and_b32_e32 v69, 0xffff, v26
	v_cmp_eq_u32_e64 s[24:25], -1, v26
	v_cndmask_b32_e64 v67, v67, 0, s[26:27]
	v_lshlrev_b32_e32 v83, 3, v67
	global_load_dwordx2 v[66:67], v66, s[58:59]
	v_cndmask_b32_e64 v69, v69, 0, s[24:25]
	v_lshlrev_b32_e32 v84, 3, v69
	v_and_b32_e32 v69, 0xffff, v2
	v_cmp_eq_u32_e64 s[22:23], -1, v2
	v_lshlrev_b32_e32 v91, 2, v70
	v_cmp_ne_u32_e64 s[20:21], -1, v35
	v_cndmask_b32_e64 v69, v69, 0, s[22:23]
	v_lshlrev_b32_e32 v85, 3, v69
	global_load_dwordx2 v[68:69], v68, s[58:59]
	s_nop 0
	global_load_dwordx2 v[70:71], v49, s[58:59]
	s_nop 0
	global_load_dwordx2 v[72:73], v72, s[58:59]
	s_nop 0
	global_load_dwordx2 v[98:99], v74, s[58:59]
	global_load_dwordx2 v[100:101], v75, s[58:59]
	global_load_dwordx2 v[102:103], v76, s[58:59]
	global_load_dwordx2 v[104:105], v77, s[58:59]
	global_load_dwordx2 v[106:107], v78, s[58:59]
	global_load_dwordx2 v[108:109], v79, s[58:59]
	global_load_dwordx2 v[110:111], v80, s[58:59]
	global_load_dwordx2 v[112:113], v81, s[58:59]
	global_load_dwordx2 v[114:115], v82, s[58:59]
	global_load_dwordx2 v[116:117], v83, s[58:59]
	global_load_dwordx2 v[118:119], v84, s[58:59]
	global_load_dwordx2 v[120:121], v85, s[58:59]
	v_bfe_u32 v49, v47, 16, 7
	s_waitcnt vmcnt(23)
	ds_add_u32 v91, v50 offset:1024
	ds_add_u32 v91, v51 offset:1792
	v_cndmask_b32_e64 v49, v49, v24, s[18:19]
	v_lshlrev_b32_e32 v49, 2, v49
	ds_add_rtn_u32 v96, v91, v25 offset:2560
	s_waitcnt vmcnt(19)
	s_andn2_b64 s[68:69], exec, s[18:19]
	s_cbranch_scc0 .Lcsk_0
	s_mov_b64 s[70:71], exec
	s_mov_b64 exec, s[68:69]
	ds_add_u32 v49, v52 offset:1024
	ds_add_u32 v49, v53 offset:1792
	ds_add_rtn_u32 v94, v49, v25 offset:2560
	s_mov_b64 exec, s[70:71]
.Lcsk_0:
	v_bfe_u32 v49, v46, 16, 7
	v_cndmask_b32_e64 v49, v49, v24, s[0:1]
	v_lshlrev_b32_e32 v49, 2, v49
	s_andn2_b64 s[68:69], exec, s[0:1]
	s_cbranch_scc0 .Lcsk_1
	s_mov_b64 s[70:71], exec
	s_mov_b64 exec, s[68:69]
	ds_add_u32 v49, v54 offset:1024
	ds_add_u32 v49, v55 offset:1792
	ds_add_rtn_u32 v92, v49, v25 offset:2560
	s_mov_b64 exec, s[70:71]
.Lcsk_1:
	v_bfe_u32 v49, v45, 16, 7
	v_cndmask_b32_e64 v49, v49, v24, s[50:51]
	v_lshlrev_b32_e32 v49, 2, v49
	s_waitcnt vmcnt(18)
	s_andn2_b64 s[68:69], exec, s[50:51]
	s_cbranch_scc0 .Lcsk_2
	s_mov_b64 s[70:71], exec
	s_mov_b64 exec, s[68:69]
	ds_add_u32 v49, v56 offset:1024
	ds_add_u32 v49, v57 offset:1792
	ds_add_rtn_u32 v89, v49, v25 offset:2560
	s_mov_b64 exec, s[70:71]
.Lcsk_2:
	v_bfe_u32 v49, v44, 16, 7
	v_cndmask_b32_e64 v49, v49, v24, s[4:5]
	v_lshlrev_b32_e32 v49, 2, v49
	s_andn2_b64 s[68:69], exec, s[4:5]
	s_cbranch_scc0 .Lcsk_3
	s_mov_b64 s[70:71], exec
	s_mov_b64 exec, s[68:69]
	ds_add_u32 v49, v58 offset:1024
	ds_add_u32 v49, v59 offset:1792
	ds_add_rtn_u32 v87, v49, v25 offset:2560
	s_mov_b64 exec, s[70:71]
.Lcsk_3:
	v_bfe_u32 v49, v43, 16, 7
	v_cndmask_b32_e64 v49, v49, v24, s[6:7]
	v_lshlrev_b32_e32 v49, 2, v49
	s_waitcnt vmcnt(17)
	s_andn2_b64 s[68:69], exec, s[6:7]
	s_cbranch_scc0 .Lcsk_4
	s_mov_b64 s[70:71], exec
	s_mov_b64 exec, s[68:69]
	ds_add_u32 v49, v60 offset:1024
	ds_add_u32 v49, v61 offset:1792
	ds_add_rtn_u32 v85, v49, v25 offset:2560
	s_mov_b64 exec, s[70:71]
.Lcsk_4:
	v_bfe_u32 v49, v42, 16, 7
	v_cndmask_b32_e64 v49, v49, v24, s[8:9]
	v_lshlrev_b32_e32 v49, 2, v49
	s_andn2_b64 s[68:69], exec, s[8:9]
	s_cbranch_scc0 .Lcsk_5
	s_mov_b64 s[70:71], exec
	s_mov_b64 exec, s[68:69]
	ds_add_u32 v49, v62 offset:1024
	ds_add_u32 v49, v63 offset:1792
	ds_add_rtn_u32 v83, v49, v25 offset:2560
	s_mov_b64 exec, s[70:71]
.Lcsk_5:
	v_bfe_u32 v49, v41, 16, 7
	v_cndmask_b32_e64 v49, v49, v24, s[10:11]
	v_lshlrev_b32_e32 v49, 2, v49
	s_waitcnt vmcnt(16)
	s_andn2_b64 s[68:69], exec, s[10:11]
	s_cbranch_scc0 .Lcsk_6
	s_mov_b64 s[70:71], exec
	s_mov_b64 exec, s[68:69]
	ds_add_u32 v49, v64 offset:1024
	ds_add_u32 v49, v65 offset:1792
	ds_add_rtn_u32 v81, v49, v25 offset:2560
	s_mov_b64 exec, s[70:71]
.Lcsk_6:
	v_bfe_u32 v49, v40, 16, 7
	v_cndmask_b32_e64 v49, v49, v24, s[12:13]
	v_lshlrev_b32_e32 v49, 2, v49
	s_waitcnt vmcnt(15)
	s_andn2_b64 s[68:69], exec, s[12:13]
	s_cbranch_scc0 .Lcsk_7
	s_mov_b64 s[70:71], exec
	s_mov_b64 exec, s[68:69]
	ds_add_u32 v49, v66 offset:1024
	ds_add_u32 v49, v67 offset:1792
	ds_add_rtn_u32 v79, v49, v25 offset:2560
	s_mov_b64 exec, s[70:71]
.Lcsk_7:
	v_bfe_u32 v49, v39, 16, 7
	v_cndmask_b32_e64 v49, v49, v24, s[14:15]
	v_lshlrev_b32_e32 v49, 2, v49
	s_waitcnt vmcnt(14)
	s_andn2_b64 s[68:69], exec, s[14:15]
	s_cbranch_scc0 .Lcsk_8
	s_mov_b64 s[70:71], exec
	s_mov_b64 exec, s[68:69]
	ds_add_u32 v49, v68 offset:1024
	ds_add_u32 v49, v69 offset:1792
	ds_add_rtn_u32 v77, v49, v25 offset:2560
	s_mov_b64 exec, s[70:71]
.Lcsk_8:
	v_bfe_u32 v49, v38, 16, 7
	v_cndmask_b32_e64 v49, v49, v24, s[16:17]
	v_lshlrev_b32_e32 v49, 2, v49
	s_waitcnt vmcnt(13)
	s_andn2_b64 s[68:69], exec, s[16:17]
	s_cbranch_scc0 .Lcsk_9
	s_mov_b64 s[70:71], exec
	s_mov_b64 exec, s[68:69]
	ds_add_u32 v49, v70 offset:1024
	ds_add_u32 v49, v71 offset:1792
	ds_add_rtn_u32 v75, v49, v25 offset:2560
	s_mov_b64 exec, s[70:71]
.Lcsk_9:
	v_bfe_u32 v49, v37, 16, 7
	v_cndmask_b32_e64 v49, v49, v24, s[48:49]
	v_lshlrev_b32_e32 v49, 2, v49
	s_waitcnt vmcnt(12)
	s_andn2_b64 s[68:69], exec, s[48:49]
	s_cbranch_scc0 .Lcsk_10
	s_mov_b64 s[70:71], exec
	s_mov_b64 exec, s[68:69]
	ds_add_u32 v49, v72 offset:1024
	ds_add_u32 v49, v73 offset:1792
	ds_add_rtn_u32 v73, v49, v25 offset:2560
	s_mov_b64 exec, s[70:71]
.Lcsk_10:
	v_bfe_u32 v49, v36, 16, 7
	v_cndmask_b32_e64 v49, v49, v24, s[46:47]
	v_lshlrev_b32_e32 v49, 2, v49
	s_waitcnt vmcnt(11)
	s_andn2_b64 s[68:69], exec, s[46:47]
	s_cbranch_scc0 .Lcsk_11
	s_mov_b64 s[70:71], exec
	s_mov_b64 exec, s[68:69]
	ds_add_u32 v49, v98 offset:1024
	ds_add_u32 v49, v99 offset:1792
	ds_add_rtn_u32 v71, v49, v25 offset:2560
	s_mov_b64 exec, s[70:71]
.Lcsk_11:
	v_bfe_u32 v49, v35, 16, 7
	v_cndmask_b32_e64 v49, v49, v24, s[44:45]
	v_lshlrev_b32_e32 v49, 2, v49
	s_waitcnt vmcnt(10)
	s_andn2_b64 s[68:69], exec, s[44:45]
	s_cbranch_scc0 .Lcsk_12
	s_mov_b64 s[70:71], exec
	s_mov_b64 exec, s[68:69]
	ds_add_u32 v49, v100 offset:1024
	ds_add_u32 v49, v101 offset:1792
	ds_add_rtn_u32 v69, v49, v25 offset:2560
	s_mov_b64 exec, s[70:71]
.Lcsk_12:
	v_bfe_u32 v49, v34, 16, 7
	v_cndmask_b32_e64 v49, v49, v24, s[42:43]
	v_lshlrev_b32_e32 v49, 2, v49
	s_waitcnt vmcnt(9)
	s_andn2_b64 s[68:69], exec, s[42:43]
	s_cbranch_scc0 .Lcsk_13
	s_mov_b64 s[70:71], exec
	s_mov_b64 exec, s[68:69]
	ds_add_u32 v49, v102 offset:1024
	ds_add_u32 v49, v103 offset:1792
	ds_add_rtn_u32 v67, v49, v25 offset:2560
	s_mov_b64 exec, s[70:71]
.Lcsk_13:
	v_bfe_u32 v49, v33, 16, 7
	v_cndmask_b32_e64 v49, v49, v24, s[40:41]
	v_lshlrev_b32_e32 v49, 2, v49
	s_waitcnt vmcnt(8)
	s_andn2_b64 s[68:69], exec, s[40:41]
	s_cbranch_scc0 .Lcsk_14
	s_mov_b64 s[70:71], exec
	s_mov_b64 exec, s[68:69]
	ds_add_u32 v49, v104 offset:1024
	ds_add_u32 v49, v105 offset:1792
	ds_add_rtn_u32 v65, v49, v25 offset:2560
	s_mov_b64 exec, s[70:71]
.Lcsk_14:
	v_bfe_u32 v49, v32, 16, 7
	v_cndmask_b32_e64 v49, v49, v24, s[38:39]
	v_lshlrev_b32_e32 v49, 2, v49
	s_waitcnt vmcnt(7)
	s_andn2_b64 s[68:69], exec, s[38:39]
	s_cbranch_scc0 .Lcsk_15
	s_mov_b64 s[70:71], exec
	s_mov_b64 exec, s[68:69]
	ds_add_u32 v49, v106 offset:1024
	ds_add_u32 v49, v107 offset:1792
	ds_add_rtn_u32 v63, v49, v25 offset:2560
	s_mov_b64 exec, s[70:71]
.Lcsk_15:
	v_bfe_u32 v49, v31, 16, 7
	v_cndmask_b32_e64 v49, v49, v24, s[36:37]
	v_lshlrev_b32_e32 v49, 2, v49
	s_waitcnt vmcnt(6)
	s_andn2_b64 s[68:69], exec, s[36:37]
	s_cbranch_scc0 .Lcsk_16
	s_mov_b64 s[70:71], exec
	s_mov_b64 exec, s[68:69]
	ds_add_u32 v49, v108 offset:1024
	ds_add_u32 v49, v109 offset:1792
	ds_add_rtn_u32 v61, v49, v25 offset:2560
	s_mov_b64 exec, s[70:71]
.Lcsk_16:
	v_bfe_u32 v49, v30, 16, 7
	v_cndmask_b32_e64 v49, v49, v24, s[34:35]
	v_lshlrev_b32_e32 v49, 2, v49
	s_waitcnt vmcnt(5)
	s_andn2_b64 s[68:69], exec, s[34:35]
	s_cbranch_scc0 .Lcsk_17
	s_mov_b64 s[70:71], exec
	s_mov_b64 exec, s[68:69]
	ds_add_u32 v49, v110 offset:1024
	ds_add_u32 v49, v111 offset:1792
	ds_add_rtn_u32 v59, v49, v25 offset:2560
	s_mov_b64 exec, s[70:71]
.Lcsk_17:
	v_bfe_u32 v49, v29, 16, 7
	v_cndmask_b32_e64 v49, v49, v24, s[30:31]
	v_lshlrev_b32_e32 v49, 2, v49
	s_waitcnt vmcnt(4)
	s_andn2_b64 s[68:69], exec, s[30:31]
	s_cbranch_scc0 .Lcsk_18
	s_mov_b64 s[70:71], exec
	s_mov_b64 exec, s[68:69]
	ds_add_u32 v49, v112 offset:1024
	ds_add_u32 v49, v113 offset:1792
	ds_add_rtn_u32 v57, v49, v25 offset:2560
	s_mov_b64 exec, s[70:71]
.Lcsk_18:
	v_bfe_u32 v49, v28, 16, 7
	v_cndmask_b32_e64 v49, v49, v24, s[28:29]
	v_lshlrev_b32_e32 v49, 2, v49
	s_waitcnt vmcnt(3)
	s_andn2_b64 s[68:69], exec, s[28:29]
	s_cbranch_scc0 .Lcsk_19
	s_mov_b64 s[70:71], exec
	s_mov_b64 exec, s[68:69]
	ds_add_u32 v49, v114 offset:1024
	ds_add_u32 v49, v115 offset:1792
	ds_add_rtn_u32 v54, v49, v25 offset:2560
	s_mov_b64 exec, s[70:71]
.Lcsk_19:
	v_bfe_u32 v49, v27, 16, 7
	v_cndmask_b32_e64 v49, v49, v24, s[26:27]
	v_lshlrev_b32_e32 v49, 2, v49
	s_waitcnt vmcnt(2)
	s_andn2_b64 s[68:69], exec, s[26:27]
	s_cbranch_scc0 .Lcsk_20
	s_mov_b64 s[70:71], exec
	s_mov_b64 exec, s[68:69]
	ds_add_u32 v49, v116 offset:1024
	ds_add_u32 v49, v117 offset:1792
	ds_add_rtn_u32 v51, v49, v25 offset:2560
	s_mov_b64 exec, s[70:71]

.Lcsk_21:
	v_lshlrev_b32_e32 v55, 2, v53
	s_andn2_b64 s[68:69], exec, s[24:25]
	s_cbranch_scc0 .Lcsk_22
	s_mov_b64 s[70:71], exec
	s_mov_b64 exec, s[68:69]
	s_mov_b64 exec, s[70:71]
.Lcsk_22:
	s_waitcnt vmcnt(0)
	s_andn2_b64 s[68:69], exec, s[22:23]
	s_cbranch_scc0 .Lcsk_23
	s_mov_b64 s[70:71], exec
	s_mov_b64 exec, s[68:69]
	ds_add_u32 v55, v120 offset:1024
	ds_add_u32 v55, v121 offset:1792
	ds_add_rtn_u32 v53, v55, v25 offset:2560
	s_mov_b64 exec, s[70:71]

.LBB2_53:
	s_waitcnt lgkmcnt(0)
	v_add_u32_e32 v96, v96, v12
	v_ashrrev_i32_e32 v97, 31, v96
	v_lshl_add_u64 v[96:97], v[96:97], 2, s[54:55]
	global_store_dword v[96:97], v48, off
	s_or_b64 exec, exec, s[66:67]
	s_and_saveexec_b64 s[50:51], s[46:47]
	s_cbranch_execz .LBB2_31
.LBB2_54:
	s_waitcnt lgkmcnt(0)
	v_add_u32_e32 v94, v94, v12
	v_ashrrev_i32_e32 v95, 31, v94
	v_lshl_add_u64 v[94:95], v[94:95], 2, s[54:55]
	global_store_dword v[94:95], v47, off
	s_or_b64 exec, exec, s[50:51]
	s_and_saveexec_b64 s[46:47], s[44:45]
	s_cbranch_execz .LBB2_32
.LBB2_55:
	s_waitcnt lgkmcnt(0)
	v_add_u32_e32 v92, v92, v12
	v_ashrrev_i32_e32 v93, 31, v92
	v_lshl_add_u64 v[92:93], v[92:93], 2, s[54:55]
	global_store_dword v[92:93], v46, off
	s_or_b64 exec, exec, s[46:47]
	s_and_saveexec_b64 s[44:45], s[42:43]
	s_cbranch_execz .LBB2_33
.LBB2_56:
	s_waitcnt lgkmcnt(0)
	v_add_u32_e32 v46, v89, v12
	v_ashrrev_i32_e32 v47, 31, v46
	v_lshl_add_u64 v[46:47], v[46:47], 2, s[54:55]
	global_store_dword v[46:47], v45, off
	s_or_b64 exec, exec, s[44:45]
	s_and_saveexec_b64 s[42:43], s[40:41]
	s_cbranch_execz .LBB2_34
.LBB2_57:
	s_waitcnt lgkmcnt(0)
	v_add_u32_e32 v46, v87, v12
	v_ashrrev_i32_e32 v47, 31, v46
	v_lshl_add_u64 v[46:47], v[46:47], 2, s[54:55]
	global_store_dword v[46:47], v44, off
	s_or_b64 exec, exec, s[42:43]
	s_and_saveexec_b64 s[40:41], s[38:39]
	s_cbranch_execz .LBB2_35
.LBB2_58:
	s_waitcnt lgkmcnt(0)
	v_add_u32_e32 v44, v85, v12
	v_ashrrev_i32_e32 v45, 31, v44
	v_lshl_add_u64 v[44:45], v[44:45], 2, s[54:55]
	global_store_dword v[44:45], v43, off
	s_or_b64 exec, exec, s[40:41]
	s_and_saveexec_b64 s[38:39], s[36:37]
	s_cbranch_execz .LBB2_36
.LBB2_59:
	s_waitcnt lgkmcnt(0)
	v_add_u32_e32 v44, v83, v12
	v_ashrrev_i32_e32 v45, 31, v44
	v_lshl_add_u64 v[44:45], v[44:45], 2, s[54:55]
	global_store_dword v[44:45], v42, off
	s_or_b64 exec, exec, s[38:39]
	s_and_saveexec_b64 s[36:37], s[34:35]
	s_cbranch_execz .LBB2_37
.LBB2_60:
	s_waitcnt lgkmcnt(0)
	v_add_u32_e32 v42, v81, v12
	v_ashrrev_i32_e32 v43, 31, v42
	v_lshl_add_u64 v[42:43], v[42:43], 2, s[54:55]
	global_store_dword v[42:43], v41, off
	s_or_b64 exec, exec, s[36:37]
	s_and_saveexec_b64 s[34:35], s[30:31]
	s_cbranch_execz .LBB2_38
.LBB2_61:
	s_waitcnt lgkmcnt(0)
	v_add_u32_e32 v42, v79, v12
	v_ashrrev_i32_e32 v43, 31, v42
	v_lshl_add_u64 v[42:43], v[42:43], 2, s[54:55]
	global_store_dword v[42:43], v40, off
	s_or_b64 exec, exec, s[34:35]
	s_and_saveexec_b64 s[30:31], s[28:29]
	s_cbranch_execz .LBB2_39
.LBB2_62:
	s_waitcnt lgkmcnt(0)
	v_add_u32_e32 v40, v77, v12
	v_ashrrev_i32_e32 v41, 31, v40
	v_lshl_add_u64 v[40:41], v[40:41], 2, s[54:55]
	global_store_dword v[40:41], v39, off
	s_or_b64 exec, exec, s[30:31]
	s_and_saveexec_b64 s[28:29], s[26:27]
	s_cbranch_execz .LBB2_40
.LBB2_63:
	s_waitcnt lgkmcnt(0)
	v_add_u32_e32 v40, v75, v12
	v_ashrrev_i32_e32 v41, 31, v40
	v_lshl_add_u64 v[40:41], v[40:41], 2, s[54:55]
	global_store_dword v[40:41], v38, off
	s_or_b64 exec, exec, s[28:29]
	s_and_saveexec_b64 s[26:27], s[24:25]
	s_cbranch_execz .LBB2_41
.LBB2_64:
	s_waitcnt lgkmcnt(0)
	v_add_u32_e32 v38, v73, v12
	v_ashrrev_i32_e32 v39, 31, v38
	v_lshl_add_u64 v[38:39], v[38:39], 2, s[54:55]
	global_store_dword v[38:39], v37, off
	s_or_b64 exec, exec, s[26:27]
	s_and_saveexec_b64 s[24:25], s[22:23]
	s_cbranch_execz .LBB2_42
.LBB2_65:
	s_waitcnt lgkmcnt(0)
	v_add_u32_e32 v38, v71, v12
	v_ashrrev_i32_e32 v39, 31, v38
	v_lshl_add_u64 v[38:39], v[38:39], 2, s[54:55]
	global_store_dword v[38:39], v36, off
	s_or_b64 exec, exec, s[24:25]
	s_and_saveexec_b64 s[22:23], s[20:21]
	s_cbranch_execz .LBB2_43
.LBB2_66:
	s_waitcnt lgkmcnt(0)
	v_add_u32_e32 v36, v69, v12
	v_ashrrev_i32_e32 v37, 31, v36
	v_lshl_add_u64 v[36:37], v[36:37], 2, s[54:55]
	global_store_dword v[36:37], v35, off
	s_or_b64 exec, exec, s[22:23]
	s_and_saveexec_b64 s[20:21], s[18:19]
	s_cbranch_execz .LBB2_44
.LBB2_67:
	s_waitcnt lgkmcnt(0)
	v_add_u32_e32 v36, v67, v12
	v_ashrrev_i32_e32 v37, 31, v36
	v_lshl_add_u64 v[36:37], v[36:37], 2, s[54:55]
	global_store_dword v[36:37], v34, off
	s_or_b64 exec, exec, s[20:21]
	s_and_saveexec_b64 s[18:19], s[16:17]
	s_cbranch_execz .LBB2_45
.LBB2_68:
	s_waitcnt lgkmcnt(0)
	v_add_u32_e32 v34, v65, v12
	v_ashrrev_i32_e32 v35, 31, v34
	v_lshl_add_u64 v[34:35], v[34:35], 2, s[54:55]
	global_store_dword v[34:35], v33, off
	s_or_b64 exec, exec, s[18:19]
	s_and_saveexec_b64 s[16:17], s[14:15]
	s_cbranch_execz .LBB2_46
.LBB2_69:
	s_waitcnt lgkmcnt(0)
	v_add_u32_e32 v34, v63, v12
	v_ashrrev_i32_e32 v35, 31, v34
	v_lshl_add_u64 v[34:35], v[34:35], 2, s[54:55]
	global_store_dword v[34:35], v32, off
	s_or_b64 exec, exec, s[16:17]
	s_and_saveexec_b64 s[14:15], s[12:13]
	s_cbranch_execz .LBB2_47
.LBB2_70:
	s_waitcnt lgkmcnt(0)
	v_add_u32_e32 v32, v61, v12
	v_ashrrev_i32_e32 v33, 31, v32
	v_lshl_add_u64 v[32:33], v[32:33], 2, s[54:55]
	global_store_dword v[32:33], v31, off
	s_or_b64 exec, exec, s[14:15]
	s_and_saveexec_b64 s[12:13], s[10:11]
	s_cbranch_execz .LBB2_48
.LBB2_71:
	s_waitcnt lgkmcnt(0)
	v_add_u32_e32 v32, v59, v12
	v_ashrrev_i32_e32 v33, 31, v32
	v_lshl_add_u64 v[32:33], v[32:33], 2, s[54:55]
	global_store_dword v[32:33], v30, off
	s_or_b64 exec, exec, s[12:13]
	s_and_saveexec_b64 s[10:11], s[8:9]
	s_cbranch_execz .LBB2_49
.LBB2_72:
	s_waitcnt lgkmcnt(0)
	v_add_u32_e32 v30, v57, v12
	v_ashrrev_i32_e32 v31, 31, v30
	v_lshl_add_u64 v[30:31], v[30:31], 2, s[54:55]
	global_store_dword v[30:31], v29, off
	s_or_b64 exec, exec, s[10:11]
	s_and_saveexec_b64 s[8:9], s[6:7]
	s_cbranch_execz .LBB2_50
.LBB2_73:
	s_waitcnt lgkmcnt(0)
	v_add_u32_e32 v30, v54, v12
	v_ashrrev_i32_e32 v31, 31, v30
	v_lshl_add_u64 v[30:31], v[30:31], 2, s[54:55]
	global_store_dword v[30:31], v28, off
	s_or_b64 exec, exec, s[8:9]
	s_and_saveexec_b64 s[6:7], s[4:5]
	s_cbranch_execz .LBB2_51
.LBB2_74:
	s_waitcnt lgkmcnt(0)
	v_add_u32_e32 v28, v51, v12
	v_ashrrev_i32_e32 v29, 31, v28
	v_lshl_add_u64 v[28:29], v[28:29], 2, s[54:55]
	global_store_dword v[28:29], v27, off
	s_or_b64 exec, exec, s[6:7]
	s_and_saveexec_b64 s[4:5], s[48:49]
	s_cbranch_execz .LBB2_52
.LBB2_75:
	s_waitcnt lgkmcnt(0)
	v_add_u32_e32 v28, v49, v12
	v_ashrrev_i32_e32 v29, 31, v28
	v_lshl_add_u64 v[28:29], v[28:29], 2, s[54:55]
	global_store_dword v[28:29], v26, off
	s_or_b64 exec, exec, s[4:5]
	s_and_saveexec_b64 s[4:5], s[0:1]
	s_cbranch_execz .LBB2_28
.LBB2_76:
	s_waitcnt lgkmcnt(0)
	v_add_u32_e32 v26, v53, v12
	v_ashrrev_i32_e32 v27, 31, v26
	v_lshl_add_u64 v[26:27], v[26:27], 2, s[54:55]
	global_store_dword v[26:27], v2, off
	s_branch .LBB2_28
